# speedup vs baseline: 1.0344x; 1.0161x over previous
.Lh_nocs:
	s_mov_b64 exec, s[6:7]
	v_subrev_u32_e32 v69, 0x100, v0
	v_cmp_gt_u32_e32 vcc, 10, v69
	s_and_saveexec_b64 s[4:5], vcc
	s_cbranch_execz .LBB2_30
	v_lshlrev_b32_e32 v21, 2, v69
	v_lshlrev_b32_e32 v18, 8, v69
	global_load_dword v20, v21, s[16:17]
	global_load_dwordx3 v[14:16], v18, s[22:23] offset:52 nt
	global_load_dwordx4 v[2:5], v18, s[22:23] offset:36 nt
	global_load_dwordx4 v[6:9], v18, s[22:23] offset:20 nt
	global_load_dwordx4 v[10:13], v18, s[22:23] offset:4 nt
	global_load_dword v19, v18, s[22:23] nt
	global_load_dword v8, v21, s[12:13]
	s_waitcnt vmcnt(0)
	v_add_u32_e32 v22, 0x7f, v20
	v_ashrrev_i32_e32 v22, 7, v22
	v_cmp_lt_i32_e32 vcc, 0, v22
	v_add_f32_e32 v19, 0, v19
	s_nop 0
	v_cndmask_b32_e32 v19, 0, v19, vcc
	v_cmp_lt_i32_e32 vcc, 1, v22
	s_nop 0
	v_cndmask_b32_e32 v10, 0, v10, vcc
	v_cmp_lt_i32_e32 vcc, 2, v22
	v_add_f32_e32 v10, v19, v10
	s_nop 0
	v_cndmask_b32_e32 v11, 0, v11, vcc
	v_cmp_lt_i32_e32 vcc, 3, v22
	v_add_f32_e32 v10, v10, v11
	s_nop 0
	v_cndmask_b32_e32 v11, 0, v12, vcc
	v_cmp_lt_i32_e32 vcc, 4, v22
	v_add_f32_e32 v10, v10, v11
	s_nop 0
	v_cndmask_b32_e32 v11, 0, v13, vcc
	v_cmp_lt_i32_e32 vcc, 5, v22
	v_add_f32_e32 v10, v10, v11
	s_nop 0
	v_cndmask_b32_e32 v6, 0, v6, vcc
	v_cmp_lt_i32_e32 vcc, 6, v22
	v_add_f32_e32 v6, v10, v6
	s_nop 0
	v_cndmask_b32_e32 v7, 0, v7, vcc
	v_cmp_lt_i32_e32 vcc, 7, v22
	v_add_f32_e32 v6, v6, v7
	s_nop 0
	v_cndmask_b32_e32 v7, 0, v8, vcc
	v_cmp_lt_i32_e32 vcc, 8, v22
	v_add_f32_e32 v6, v6, v7
	s_nop 0
	v_cndmask_b32_e32 v7, 0, v9, vcc
	v_cmp_lt_i32_e32 vcc, 9, v22
	v_add_f32_e32 v6, v6, v7
	s_nop 0
	v_cndmask_b32_e32 v2, 0, v2, vcc
	v_cmp_lt_i32_e32 vcc, 10, v22
	v_add_f32_e32 v2, v6, v2
	s_nop 0
	v_cndmask_b32_e32 v3, 0, v3, vcc
	v_cmp_lt_i32_e32 vcc, 11, v22
	v_add_f32_e32 v2, v2, v3
	s_nop 0
	v_cndmask_b32_e32 v3, 0, v4, vcc
	v_cmp_lt_i32_e32 vcc, 12, v22
	v_add_f32_e32 v2, v2, v3
	s_nop 0
	v_cndmask_b32_e32 v3, 0, v5, vcc
	v_cmp_lt_i32_e32 vcc, 13, v22
	v_add_f32_e32 v2, v2, v3
	s_nop 0
	v_cndmask_b32_e32 v3, 0, v14, vcc
	v_cmp_lt_i32_e32 vcc, 14, v22
	v_add_f32_e32 v2, v2, v3
	s_nop 0
	v_cndmask_b32_e32 v3, 0, v15, vcc
	v_cmp_lt_i32_e32 vcc, 15, v22
	v_add_f32_e32 v2, v2, v3
	s_nop 0
	v_cndmask_b32_e32 v3, 0, v16, vcc
	v_add_f32_e32 v4, v2, v3
	v_cmp_lt_i32_e32 vcc, 16, v22
	s_and_saveexec_b64 s[6:7], vcc
	s_cbranch_execz .LBB2_29
	v_mov_b32_e32 v19, 0
	v_lshl_add_u64 v[2:3], s[22:23], 0, v[18:19]
	v_lshl_add_u64 v[2:3], v[2:3], 0, 64
	v_add_u32_e32 v5, -16, v22
	s_mov_b64 s[22:23], 0

.LBB2_29:
	s_or_b64 exec, exec, s[6:7]
	v_cvt_f32_i32_e32 v2, v20
	v_div_scale_f32 v3, s[6:7], v2, v2, v4
	v_rcp_f32_e32 v5, v3
	s_nop 0
	v_fma_f32 v6, -v3, v5, 1.0
	v_fmac_f32_e32 v5, v6, v5
	v_div_scale_f32 v6, vcc, v4, v2, v4
	v_mul_f32_e32 v7, v6, v5
	v_fma_f32 v9, -v3, v7, v6
	v_fmac_f32_e32 v7, v9, v5
	v_fma_f32 v3, -v3, v7, v6
	v_div_fmas_f32 v3, v3, v5, v7
	v_div_fixup_f32 v9, v3, v2, v4
	s_waitcnt vmcnt(0)
	ds_write_b32 v21, v9 offset:29760
	ds_write_b32 v21, v8 offset:30272

.LBB2_32:
	s_or_b64 exec, exec, s[34:35]
	s_waitcnt lgkmcnt(0)
	s_barrier
	v_lshlrev_b32_e32 v10, 2, v0
	s_mov_b64 s[6:7], exec
	s_and_b64 exec, exec, s[0:1]
	s_cbranch_execz .Lsp_nr
	ds_read_b32 v9, v10 offset:29760
	ds_read_b32 v8, v10 offset:30272
.Lsp_nr:
	s_mov_b64 exec, s[6:7]
	v_readfirstlane_b32 s3, v17
	s_cmp_gt_u32 s3, 7
	s_cbranch_scc1 .Lmf_skip
	v_and_b32_e32 v2, 15, v1
	v_lshrrev_b32_e32 v3, 4, v1
	v_mul_u32_u24_e32 v5, 0x410, v2
	v_lshl_add_u32 v5, v3, 5, v5
	s_lshl_b32 s8, s3, 7
	s_lshl_b32 s9, s3, 9
	s_add_u32 s9, s9, 0x5140
	v_add_u32_e32 v5, s8, v5
	ds_read_b128 v[18:21], v5
	ds_read_b128 v[26:29], v5 offset:10400
	ds_read_b128 v[22:25], v5 offset:16
	ds_read_b128 v[30:33], v5 offset:10416
	v_mul_u32_u24_e32 v11, 0xa0, v3
	v_lshl_add_u32 v11, v2, 2, v11
	v_add_u32_e32 v11, s9, v11
	v_cmp_gt_u32_e64 s[10:11], 10, v2
	v_cmp_gt_u32_e64 s[12:13], 3, v3
	v_cmp_gt_u32_e64 s[14:15], 2, v3
	s_and_b64 s[12:13], s[10:11], s[12:13]
	s_and_b64 s[14:15], s[10:11], s[14:15]
	s_waitcnt lgkmcnt(3)
	v_mfma_f32_16x16x4_f32 v[34:37], v18, v18, 0
	s_waitcnt lgkmcnt(2)
	v_mfma_f32_16x16x4_f32 v[38:41], v26, v26, 0
	v_mfma_f32_16x16x4_f32 v[34:37], v19, v19, v[34:37]
	v_mfma_f32_16x16x4_f32 v[38:41], v27, v27, v[38:41]
	v_mfma_f32_16x16x4_f32 v[34:37], v20, v20, v[34:37]
	v_mfma_f32_16x16x4_f32 v[38:41], v28, v28, v[38:41]
	v_mfma_f32_16x16x4_f32 v[34:37], v21, v21, v[34:37]
	v_mfma_f32_16x16x4_f32 v[38:41], v29, v29, v[38:41]
	s_waitcnt lgkmcnt(0)
	v_mfma_f32_16x16x4_f32 v[34:37], v22, v22, v[34:37]
	v_mfma_f32_16x16x4_f32 v[38:41], v30, v30, v[38:41]
	v_mfma_f32_16x16x4_f32 v[34:37], v23, v23, v[34:37]
	v_mfma_f32_16x16x4_f32 v[38:41], v31, v31, v[38:41]
	v_mfma_f32_16x16x4_f32 v[34:37], v24, v24, v[34:37]
	v_mfma_f32_16x16x4_f32 v[38:41], v32, v32, v[38:41]
	v_mfma_f32_16x16x4_f32 v[34:37], v25, v25, v[34:37]
	v_mfma_f32_16x16x4_f32 v[38:41], v33, v33, v[38:41]
	s_nop 11
	s_mov_b64 s[6:7], exec
	s_mov_b64 exec, s[12:13]
	ds_write_b32 v11, v34
	ds_write_b32 v11, v35 offset:40
	ds_write_b32 v11, v38 offset:4096
	ds_write_b32 v11, v39 offset:4136
	s_mov_b64 exec, s[14:15]
	ds_write_b32 v11, v36 offset:80
	ds_write_b32 v11, v37 offset:120
	ds_write_b32 v11, v40 offset:4176
	ds_write_b32 v11, v41 offset:4216
	s_mov_b64 exec, s[6:7]
